# baseline (speedup 1.0000x reference)
.LBB3_9:
	ds_read_b128 v[146:149], v150
	ds_read_b128 v[156:159], v150 offset:2048
	ds_read_b128 v[170:173], v154
	ds_read_b128 v[174:177], v154 offset:2048
	s_mov_b32 s65, s54
	s_mov_b32 s54, s66
	ds_read_b128 v[138:141], v163
	ds_read_b128 v[126:129], v163 offset:2048
	ds_read_b128 v[142:145], v164
	ds_read_b128 v[130:133], v164 offset:2048
	ds_read_b128 v[122:125], v163 offset:4096
	ds_read_b128 v[114:117], v163 offset:6144
	ds_read_b128 v[134:137], v164 offset:4096
	ds_read_b128 v[118:121], v164 offset:6144
	s_waitcnt vmcnt(10)
	s_mul_i32 s21, s52, s22
	s_lshl_b32 s20, s27, 6
	v_add_u32_e32 v169, s65, v1
	ds_write_b128 v1, v[22:25] offset:16384
	ds_write_b128 v1, v[18:21] offset:24576
	s_nop 0
	s_add_i32 s66, s21, s20
	s_lshl_b32 s66, s66, 1
	s_add_i32 s67, s66, s51
	buffer_load_dwordx4 v[22:25], v162, s[0:3], s66 offen
	buffer_load_dwordx4 v[18:21], v162, s[0:3], s67 offen
	s_waitcnt vmcnt(10)
	ds_write_b128 v169, v[14:17] offset:32768
	ds_write_b128 v169, v[10:13] offset:40960
	s_nop 0
	s_mul_i32 s66, s53, s22
	s_add_i32 s67, s66, s20
	s_lshl_b32 s67, s67, 1
	s_add_i32 s68, s67, s51
	s_nop 0
	s_barrier
	s_waitcnt lgkmcnt(0)
	s_setprio 1
	s_waitcnt lgkmcnt(11)
	v_mfma_f32_16x16x32_f16 v[110:113], v[146:149], v[138:141], v[110:113]
	v_mfma_f32_16x16x32_f16 v[106:109], v[156:159], v[138:141], v[106:109]
	s_waitcnt lgkmcnt(10)
	v_mfma_f32_16x16x32_f16 v[102:105], v[146:149], v[126:129], v[102:105]
	v_mfma_f32_16x16x32_f16 v[98:101], v[156:159], v[126:129], v[98:101]
	s_waitcnt lgkmcnt(7)
	v_mfma_f32_16x16x32_f16 v[94:97], v[146:149], v[122:125], v[94:97]
	v_mfma_f32_16x16x32_f16 v[90:93], v[156:159], v[122:125], v[90:93]
	s_waitcnt lgkmcnt(6)
	v_mfma_f32_16x16x32_f16 v[86:89], v[146:149], v[114:117], v[86:89]
	v_mfma_f32_16x16x32_f16 v[82:85], v[156:159], v[114:117], v[82:85]
	v_mfma_f32_16x16x32_f16 v[110:113], v[170:173], v[142:145], v[110:113]
	v_mfma_f32_16x16x32_f16 v[106:109], v[174:177], v[142:145], v[106:109]
	v_mfma_f32_16x16x32_f16 v[102:105], v[170:173], v[130:133], v[102:105]
	v_mfma_f32_16x16x32_f16 v[98:101], v[174:177], v[130:133], v[98:101]
	s_waitcnt lgkmcnt(5)
	v_mfma_f32_16x16x32_f16 v[94:97], v[170:173], v[134:137], v[94:97]
	v_mfma_f32_16x16x32_f16 v[90:93], v[174:177], v[134:137], v[90:93]
	s_waitcnt lgkmcnt(4)
	v_mfma_f32_16x16x32_f16 v[86:89], v[170:173], v[118:121], v[86:89]
	v_mfma_f32_16x16x32_f16 v[82:85], v[174:177], v[118:121], v[82:85]
	s_setprio 0
	s_barrier
	ds_read_b128 v[146:149], v150 offset:16384
	ds_read_b128 v[150:153], v150 offset:18432
	ds_read_b128 v[158:161], v154 offset:16384
	ds_read_b128 v[154:157], v154 offset:18432
	s_waitcnt vmcnt(8)
	buffer_load_dwordx4 v[14:17], v162, s[28:31], s67 offen
	buffer_load_dwordx4 v[10:13], v162, s[28:31], s68 offen
	s_add_i32 s67, s66, s51
	s_add_i32 s20, s67, s20
	s_lshl_b32 s20, s20, 1
	ds_write_b128 v169, v[6:9] offset:49152
	ds_write_b128 v169, v[2:5] offset:57344
	s_add_i32 s68, s20, s51
	s_nop 4
	buffer_load_dwordx4 v[6:9], v162, s[28:31], s20 offen
	buffer_load_dwordx4 v[2:5], v162, s[28:31], s68 offen
	s_add_i32 s27, s27, 1
	s_cmp_eq_u32 s27, s55
	s_cbranch_scc0 .LBB3_13
	s_add_i32 s20, s64, 1
	s_cmp_gt_i32 s64, -1
	s_cbranch_scc1 .LBB3_12
	s_mul_i32 s0, s20, s33
	s_add_i32 s0, s0, s44
	s_abs_i32 s21, s0
	s_mul_hi_u32 s27, s21, s46
	s_mul_i32 s28, s27, s43
	s_ashr_i32 s1, s0, 31
	s_sub_i32 s21, s21, s28
	s_xor_b32 s1, s1, s45
	s_add_i32 s28, s27, 1
	s_sub_i32 s29, s21, s43
	s_cmp_ge_u32 s21, s43
	s_cselect_b32 s27, s28, s27
	s_cselect_b32 s21, s29, s21
	s_add_i32 s28, s27, 1
	s_cmp_ge_u32 s21, s43
	s_cselect_b32 s21, s28, s27
	s_xor_b32 s21, s21, s1
	s_sub_i32 s1, s21, s1
	s_mul_i32 s21, s1, s42
	s_sub_i32 s0, s0, s21
	s_abs_i32 s27, s0
	s_mul_hi_u32 s28, s27, s49
	s_mul_i32 s29, s28, s47
	s_ashr_i32 s21, s0, 31
	s_sub_i32 s27, s27, s29
	s_xor_b32 s21, s21, s48
	s_add_i32 s29, s28, 1
	s_sub_i32 s30, s27, s47
	s_cmp_ge_u32 s27, s47
	s_cselect_b32 s28, s29, s28
	s_cselect_b32 s27, s30, s27
	s_add_i32 s29, s28, 1
	s_cmp_ge_u32 s27, s47
	s_cselect_b32 s27, s29, s28
	s_xor_b32 s27, s27, s21
	s_sub_i32 s21, s27, s21
	s_lshl_b32 s52, s21, 7
	s_mul_i32 s21, s21, s23
	s_sub_i32 s0, s0, s21
	s_lshl_b32 s53, s0, 8
	s_cmp_eq_u32 s1, 1
	s_cselect_b32 s21, s7, s9
	s_cselect_b32 s0, s6, s8
	s_cselect_b32 s27, s13, s15
	s_cselect_b32 s28, s12, s14
	s_cmp_eq_u32 s1, 0
	s_cselect_b32 s1, s5, s21
	s_cselect_b32 s21, s11, s27
	s_mov_b32 s27, s3
	s_mul_i32 s66, s53, s22
	s_cselect_b32 s0, s4, s0
	s_cselect_b32 s28, s10, s28
	s_and_b32 s1, s1, 0xffff
	s_and_b32 s29, s21, 0xffff
	s_mul_i32 s21, s52, s22
	s_add_i32 s67, s66, s51
	s_mov_b64 s[30:31], s[26:27]

.LBB3_14:
	s_barrier
	s_waitcnt lgkmcnt(0)
	s_setprio 1
	s_waitcnt lgkmcnt(5)
	v_mfma_f32_16x16x32_f16 v[78:81], v[146:149], v[138:141], v[78:81]
	s_waitcnt lgkmcnt(4)
	v_mfma_f32_16x16x32_f16 v[74:77], v[150:153], v[138:141], v[74:77]
	v_mfma_f32_16x16x32_f16 v[70:73], v[146:149], v[126:129], v[70:73]
	v_mfma_f32_16x16x32_f16 v[66:69], v[150:153], v[126:129], v[66:69]
	v_mfma_f32_16x16x32_f16 v[62:65], v[146:149], v[122:125], v[62:65]
	v_mfma_f32_16x16x32_f16 v[58:61], v[150:153], v[122:125], v[58:61]
	v_mfma_f32_16x16x32_f16 v[54:57], v[146:149], v[114:117], v[54:57]
	v_mfma_f32_16x16x32_f16 v[50:53], v[150:153], v[114:117], v[50:53]
	s_waitcnt lgkmcnt(3)
	v_mfma_f32_16x16x32_f16 v[78:81], v[158:161], v[142:145], v[78:81]
	s_waitcnt lgkmcnt(2)
	v_mfma_f32_16x16x32_f16 v[74:77], v[154:157], v[142:145], v[74:77]
	v_mfma_f32_16x16x32_f16 v[70:73], v[158:161], v[130:133], v[70:73]
	v_mfma_f32_16x16x32_f16 v[66:69], v[154:157], v[130:133], v[66:69]
	v_mfma_f32_16x16x32_f16 v[62:65], v[158:161], v[134:137], v[62:65]
	v_mfma_f32_16x16x32_f16 v[58:61], v[154:157], v[134:137], v[58:61]
	v_mfma_f32_16x16x32_f16 v[54:57], v[158:161], v[118:121], v[54:57]
	v_mfma_f32_16x16x32_f16 v[50:53], v[154:157], v[118:121], v[50:53]
	s_setprio 0
	s_barrier
	v_add_u32_e32 v169, s65, v165
	v_add_u32_e32 v170, s65, v168
	ds_read_b128 v[146:149], v169 offset:32768
	ds_read_b128 v[150:153], v169 offset:34816
	ds_read_b128 v[154:157], v170 offset:32768
	ds_read_b128 v[158:161], v170 offset:34816
	ds_read_b128 v[138:141], v163 offset:16384
	ds_read_b128 v[126:129], v163 offset:18432
	ds_read_b128 v[142:145], v164 offset:16384
	ds_read_b128 v[130:133], v164 offset:18432
	ds_read_b128 v[122:125], v163 offset:20480
	ds_read_b128 v[114:117], v163 offset:22528
	ds_read_b128 v[134:137], v164 offset:20480
	ds_read_b128 v[118:121], v164 offset:22528
	s_waitcnt vmcnt(10)
	s_lshl_b32 s64, s27, 6
	v_add_u32_e32 v171, s62, v1
	s_add_i32 s21, s21, s64
	ds_write_b128 v1, v[46:49]
	ds_write_b128 v1, v[42:45] offset:8192
	s_nop 0
	s_lshl_b32 s21, s21, 1
	s_add_i32 s68, s21, s51
	buffer_load_dwordx4 v[46:49], v162, s[0:3], s21 offen
	buffer_load_dwordx4 v[42:45], v162, s[0:3], s68 offen
	s_waitcnt vmcnt(10)
	ds_write_b128 v171, v[38:41] offset:32768
	ds_write_b128 v171, v[34:37] offset:40960
	s_nop 0
	s_add_i32 s21, s66, s64
	s_lshl_b32 s21, s21, 1
	s_add_i32 s66, s21, s51
	s_nop 0
	s_barrier
	s_waitcnt lgkmcnt(0)
	s_setprio 1
	s_waitcnt lgkmcnt(11)
	v_mfma_f32_16x16x32_f16 v[110:113], v[146:149], v[138:141], v[110:113]
	v_mfma_f32_16x16x32_f16 v[106:109], v[150:153], v[138:141], v[106:109]
	s_waitcnt lgkmcnt(10)
	v_mfma_f32_16x16x32_f16 v[102:105], v[146:149], v[126:129], v[102:105]
	v_mfma_f32_16x16x32_f16 v[98:101], v[150:153], v[126:129], v[98:101]
	s_waitcnt lgkmcnt(7)
	v_mfma_f32_16x16x32_f16 v[94:97], v[146:149], v[122:125], v[94:97]
	v_mfma_f32_16x16x32_f16 v[90:93], v[150:153], v[122:125], v[90:93]
	s_waitcnt lgkmcnt(6)
	v_mfma_f32_16x16x32_f16 v[86:89], v[146:149], v[114:117], v[86:89]
	v_mfma_f32_16x16x32_f16 v[82:85], v[150:153], v[114:117], v[82:85]
	v_mfma_f32_16x16x32_f16 v[110:113], v[154:157], v[142:145], v[110:113]
	v_mfma_f32_16x16x32_f16 v[106:109], v[158:161], v[142:145], v[106:109]
	v_mfma_f32_16x16x32_f16 v[102:105], v[154:157], v[130:133], v[102:105]
	v_mfma_f32_16x16x32_f16 v[98:101], v[158:161], v[130:133], v[98:101]
	s_waitcnt lgkmcnt(5)
	v_mfma_f32_16x16x32_f16 v[94:97], v[154:157], v[134:137], v[94:97]
	v_mfma_f32_16x16x32_f16 v[90:93], v[158:161], v[134:137], v[90:93]
	s_waitcnt lgkmcnt(4)
	v_mfma_f32_16x16x32_f16 v[86:89], v[154:157], v[118:121], v[86:89]
	v_mfma_f32_16x16x32_f16 v[82:85], v[158:161], v[118:121], v[82:85]
	s_setprio 0
	s_barrier
	ds_read_b128 v[146:149], v169 offset:49152
	ds_read_b128 v[150:153], v169 offset:51200
	ds_read_b128 v[158:161], v170 offset:49152
	ds_read_b128 v[154:157], v170 offset:51200
	s_waitcnt vmcnt(8)
	buffer_load_dwordx4 v[38:41], v162, s[28:31], s21 offen
	buffer_load_dwordx4 v[34:37], v162, s[28:31], s66 offen
	s_add_i32 s21, s67, s64
	s_lshl_b32 s21, s21, 1
	s_add_i32 s64, s21, s51
	ds_write_b128 v171, v[30:33] offset:49152
	ds_write_b128 v171, v[26:29] offset:57344
	s_nop 4
	buffer_load_dwordx4 v[30:33], v162, s[28:31], s21 offen
	buffer_load_dwordx4 v[26:29], v162, s[28:31], s64 offen
	s_add_i32 s27, s27, 1
	s_cmp_lg_u32 s27, s55
	s_cbranch_scc1 .LBB3_18
	s_add_i32 s64, s20, 1
	s_cmp_gt_i32 s20, -1
	s_cbranch_scc1 .LBB3_17
	s_mul_i32 s0, s64, s33
	s_add_i32 s0, s0, s44
	s_abs_i32 s20, s0
	s_mul_hi_u32 s21, s20, s46
	s_mul_i32 s27, s21, s43
	s_ashr_i32 s1, s0, 31
	s_sub_i32 s20, s20, s27
	s_xor_b32 s1, s1, s45
	s_add_i32 s27, s21, 1
	s_sub_i32 s28, s20, s43
	s_cmp_ge_u32 s20, s43
	s_cselect_b32 s21, s27, s21
	s_cselect_b32 s20, s28, s20
	s_add_i32 s27, s21, 1
	s_cmp_ge_u32 s20, s43
	s_cselect_b32 s20, s27, s21
	s_xor_b32 s20, s20, s1
	s_sub_i32 s1, s20, s1
	s_mul_i32 s20, s1, s42
	s_sub_i32 s0, s0, s20
	s_abs_i32 s21, s0
	s_mul_hi_u32 s27, s21, s49
	s_mul_i32 s28, s27, s47
	s_ashr_i32 s20, s0, 31
	s_sub_i32 s21, s21, s28
	s_xor_b32 s20, s20, s48
	s_add_i32 s28, s27, 1
	s_sub_i32 s29, s21, s47
	s_cmp_ge_u32 s21, s47
	s_cselect_b32 s27, s28, s27
	s_cselect_b32 s21, s29, s21
	s_add_i32 s28, s27, 1
	s_cmp_ge_u32 s21, s47
	s_cselect_b32 s21, s28, s27
	s_xor_b32 s21, s21, s20
	s_sub_i32 s20, s21, s20
	s_lshl_b32 s52, s20, 7
	s_mul_i32 s20, s20, s23
	s_sub_i32 s0, s0, s20
	s_lshl_b32 s53, s0, 8
	s_cmp_eq_u32 s1, 1
	s_cselect_b32 s20, s7, s9
	s_cselect_b32 s0, s6, s8
	s_cselect_b32 s21, s13, s15
	s_cselect_b32 s27, s12, s14
	s_cmp_eq_u32 s1, 0
	s_cselect_b32 s1, s5, s20
	s_cselect_b32 s28, s10, s27
	s_cselect_b32 s20, s11, s21
	s_mov_b32 s27, s3
	s_cselect_b32 s0, s4, s0
	s_and_b32 s1, s1, 0xffff
	s_and_b32 s29, s20, 0xffff
	s_mov_b64 s[30:31], s[26:27]
